# stack4 + scan step v_pk_mul_f32 split into scalar v_mul_f32 pairs beside the MFMAs (strategy 7, bit-identical)
# baseline (speedup 1.0000x reference)
.LBB0_599:
	ds_read_b128 v[154:157], v133
	ds_read_b128 v[158:161], v133 offset:64
	ds_read_b128 v[162:165], v133 offset:2560
	ds_read_b128 v[166:169], v133 offset:2624
	ds_read_b128 v[170:173], v133 offset:5120
	ds_read_b128 v[174:177], v133 offset:5184
	ds_read_b128 v[178:181], v133 offset:7680
	ds_read_b128 v[182:185], v133 offset:7744
	ds_read_b128 v[186:189], v135
	ds_read_b128 v[190:193], v135 offset:64
	ds_read_b128 v[194:197], v135 offset:8704
	ds_read_b128 v[198:201], v135 offset:8768
	ds_read_b128 v[202:205], v135 offset:17408
	ds_read_b128 v[206:209], v135 offset:17472
	ds_read_b128 v[210:213], v135 offset:26112
	ds_read_b128 v[216:219], v135 offset:26176
	s_waitcnt vmcnt(12) lgkmcnt(14)
	v_mfma_f32_16x16x32_bf16 v[154:157], v[154:157], v[46:49], 0
	s_waitcnt vmcnt(11)
	v_mfma_f32_16x16x32_bf16 v[154:157], v[158:161], v[30:33], v[154:157]
	s_waitcnt lgkmcnt(13)
	v_mfma_f32_16x16x32_bf16 v[158:161], v[162:165], v[46:49], 0
	s_waitcnt lgkmcnt(12)
	v_mfma_f32_16x16x32_bf16 v[158:161], v[166:169], v[30:33], v[158:161]
	s_waitcnt lgkmcnt(11)
	v_mfma_f32_16x16x32_bf16 v[162:165], v[170:173], v[46:49], 0
	s_waitcnt lgkmcnt(9)
	v_mfma_f32_16x16x32_bf16 v[166:169], v[178:181], v[46:49], 0
	v_mfma_f32_16x16x32_bf16 v[162:165], v[174:177], v[30:33], v[162:165]
	s_waitcnt lgkmcnt(8)
	v_mfma_f32_16x16x32_bf16 v[166:169], v[182:185], v[30:33], v[166:169]
	ds_read_b128 v[170:173], v135 offset:128
	ds_read_b128 v[174:177], v135 offset:192
	ds_read_b128 v[178:181], v135 offset:8832
	ds_read_b128 v[182:185], v135 offset:8896
	ds_read_b128 v[220:223], v135 offset:17536
	ds_read_b128 v[224:227], v135 offset:17600
	ds_read_b128 v[228:231], v135 offset:26240
	ds_read_b128 v[232:235], v135 offset:26304
	v_cvt_pk_bf16_f32 v236, v106, v107
	v_cvt_pk_bf16_f32 v237, v108, v109
	v_cvt_pk_bf16_f32 v238, v102, v103
	v_cvt_pk_bf16_f32 v239, v104, v105
	s_waitcnt lgkmcnt(14)
	v_mfma_f32_16x16x32_bf16 v[154:157], v[186:189], v[236:239], v[154:157]
	v_cvt_pk_bf16_f32 v186, v98, v99
	v_cvt_pk_bf16_f32 v187, v100, v101
	v_cvt_pk_bf16_f32 v188, v94, v95
	s_waitcnt lgkmcnt(13)
	v_mfma_f32_16x16x32_bf16 v[158:161], v[194:197], v[236:239], v[158:161]
	v_cvt_pk_bf16_f32 v189, v96, v97
	s_waitcnt lgkmcnt(11)
	v_mfma_f32_16x16x32_bf16 v[162:165], v[202:205], v[236:239], v[162:165]
	s_waitcnt lgkmcnt(9)
	v_mfma_f32_16x16x32_bf16 v[166:169], v[210:213], v[236:239], v[166:169]
	v_mfma_f32_16x16x32_bf16 v[154:157], v[190:193], v[186:189], v[154:157]
	v_mfma_f32_16x16x32_bf16 v[158:161], v[198:201], v[186:189], v[158:161]
	v_mfma_f32_16x16x32_bf16 v[162:165], v[206:209], v[186:189], v[162:165]
	s_waitcnt lgkmcnt(8)
	v_mfma_f32_16x16x32_bf16 v[166:169], v[216:219], v[186:189], v[166:169]
	ds_read_b128 v[186:189], v135 offset:256
	ds_read_b128 v[190:193], v135 offset:320
	ds_read_b128 v[194:197], v135 offset:8960
	ds_read_b128 v[198:201], v135 offset:9024
	ds_read_b128 v[202:205], v135 offset:17664
	ds_read_b128 v[206:209], v135 offset:17728
	ds_read_b128 v[210:213], v135 offset:26368
	ds_read_b128 v[216:219], v135 offset:26432
	v_cvt_pk_bf16_f32 v236, v90, v91
	v_cvt_pk_bf16_f32 v237, v92, v93
	v_cvt_pk_bf16_f32 v238, v86, v87
	v_cvt_pk_bf16_f32 v239, v88, v89
	s_waitcnt lgkmcnt(14)
	v_mfma_f32_16x16x32_bf16 v[154:157], v[170:173], v[236:239], v[154:157]
	v_cvt_pk_bf16_f32 v170, v82, v83
	v_cvt_pk_bf16_f32 v171, v84, v85
	v_cvt_pk_bf16_f32 v172, v78, v79
	s_waitcnt lgkmcnt(13)
	v_mfma_f32_16x16x32_bf16 v[158:161], v[178:181], v[236:239], v[158:161]
	v_cvt_pk_bf16_f32 v173, v80, v81
	s_waitcnt lgkmcnt(11)
	v_mfma_f32_16x16x32_bf16 v[162:165], v[220:223], v[236:239], v[162:165]
	s_waitcnt lgkmcnt(9)
	v_mfma_f32_16x16x32_bf16 v[166:169], v[228:231], v[236:239], v[166:169]
	v_mfma_f32_16x16x32_bf16 v[154:157], v[174:177], v[170:173], v[154:157]
	v_mfma_f32_16x16x32_bf16 v[158:161], v[182:185], v[170:173], v[158:161]
	v_mfma_f32_16x16x32_bf16 v[162:165], v[224:227], v[170:173], v[162:165]
	s_waitcnt lgkmcnt(8)
	v_mfma_f32_16x16x32_bf16 v[166:169], v[232:235], v[170:173], v[166:169]
	ds_read_b128 v[170:173], v135 offset:384
	ds_read_b128 v[174:177], v135 offset:448
	ds_read_b128 v[178:181], v135 offset:9088
	ds_read_b128 v[182:185], v135 offset:9152
	ds_read_b128 v[220:223], v135 offset:17792
	ds_read_b128 v[224:227], v135 offset:17856
	ds_read_b128 v[228:231], v135 offset:26496
	ds_read_b128 v[232:235], v135 offset:26560
	v_cvt_pk_bf16_f32 v236, v74, v75
	v_cvt_pk_bf16_f32 v237, v76, v77
	v_cvt_pk_bf16_f32 v238, v70, v71
	v_cvt_pk_bf16_f32 v239, v72, v73
	s_waitcnt lgkmcnt(14)
	v_mfma_f32_16x16x32_bf16 v[154:157], v[186:189], v[236:239], v[154:157]
	v_cvt_pk_bf16_f32 v186, v66, v67
	v_cvt_pk_bf16_f32 v187, v68, v69
	v_cvt_pk_bf16_f32 v188, v62, v63
	s_waitcnt lgkmcnt(13)
	v_mfma_f32_16x16x32_bf16 v[158:161], v[194:197], v[236:239], v[158:161]
	v_cvt_pk_bf16_f32 v189, v64, v65
	s_waitcnt lgkmcnt(11)
	v_mfma_f32_16x16x32_bf16 v[162:165], v[202:205], v[236:239], v[162:165]
	s_waitcnt lgkmcnt(9)
	v_mfma_f32_16x16x32_bf16 v[166:169], v[210:213], v[236:239], v[166:169]
	v_mfma_f32_16x16x32_bf16 v[154:157], v[190:193], v[186:189], v[154:157]
	v_mfma_f32_16x16x32_bf16 v[158:161], v[198:201], v[186:189], v[158:161]
	v_mfma_f32_16x16x32_bf16 v[162:165], v[206:209], v[186:189], v[162:165]
	s_waitcnt lgkmcnt(8)
	v_mfma_f32_16x16x32_bf16 v[166:169], v[216:219], v[186:189], v[166:169]
	ds_read_b128 v[186:189], v134 offset:34816
	ds_read_b128 v[190:193], v134 offset:34880
	ds_read_b128 v[194:197], v137
	ds_read_b128 v[198:201], v137 offset:16
	ds_read_b128 v[202:205], v134 offset:37376
	ds_read_b128 v[206:209], v134 offset:37440
	ds_read_b128 v[210:213], v134 offset:39936
	ds_read_b128 v[216:219], v134 offset:40000
	ds_read_b128 v[236:239], v134 offset:42496
	ds_read_b128 v[240:243], v134 offset:42560
	ds_read_b128 v[244:247], v137 offset:128
	ds_read_b128 v[248:251], v137 offset:144
	v_cvt_pk_bf16_f32 v126, v58, v59
	v_cvt_pk_bf16_f32 v127, v60, v61
	v_cvt_pk_bf16_f32 v128, v54, v55
	v_cvt_pk_bf16_f32 v129, v56, v57
	s_waitcnt lgkmcnt(14)
	v_mfma_f32_16x16x32_bf16 v[154:157], v[170:173], v[126:129], v[154:157]
	v_mfma_f32_16x16x32_bf16 v[158:161], v[178:181], v[126:129], v[158:161]
	v_mfma_f32_16x16x32_bf16 v[162:165], v[220:223], v[126:129], v[162:165]
	s_waitcnt lgkmcnt(13)
	v_mfma_f32_16x16x32_bf16 v[126:129], v[228:231], v[126:129], v[166:169]
	v_cvt_pk_bf16_f32 v166, v50, v51
	v_cvt_pk_bf16_f32 v167, v52, v53
	v_cvt_pk_bf16_f32 v168, v110, v111
	v_cvt_pk_bf16_f32 v169, v112, v113
	s_nop 0
	v_mfma_f32_16x16x32_bf16 v[154:157], v[174:177], v[166:169], v[154:157]
	v_mfma_f32_16x16x32_bf16 v[158:161], v[182:185], v[166:169], v[158:161]
	v_mfma_f32_16x16x32_bf16 v[162:165], v[224:227], v[166:169], v[162:165]
	s_waitcnt lgkmcnt(12)
	v_mfma_f32_16x16x32_bf16 v[126:129], v[232:235], v[166:169], v[126:129]
	s_bitcmp1_b32 s9, 0
	s_cselect_b32 s9, 0x4400, 0
	v_add_u32_e32 v166, s9, v143
	v_cvt_pk_bf16_f32 v154, v154, v155
	v_cvt_pk_bf16_f32 v155, v156, v157
	s_nop 0
	ds_write_b16 v166, v154
	ds_write_b16_d16_hi v166, v154 offset:272
	ds_write_b16 v166, v155 offset:544
	ds_write_b16_d16_hi v166, v155 offset:816
	v_cvt_pk_bf16_f32 v154, v158, v159
	v_cvt_pk_bf16_f32 v155, v160, v161
	ds_write_b16 v166, v154 offset:4352
	ds_write_b16_d16_hi v166, v154 offset:4624
	ds_write_b16 v166, v155 offset:4896
	ds_write_b16_d16_hi v166, v155 offset:5168
	v_cvt_pk_bf16_f32 v154, v162, v163
	v_cvt_pk_bf16_f32 v155, v164, v165
	ds_write_b16 v166, v154 offset:8704
	ds_write_b16_d16_hi v166, v154 offset:8976
	ds_write_b16 v166, v155 offset:9248
	ds_write_b16_d16_hi v166, v155 offset:9520
	v_cvt_pk_bf16_f32 v126, v126, v127
	v_cvt_pk_bf16_f32 v127, v128, v129
	ds_write_b16 v166, v126 offset:13056
	ds_write_b16_d16_hi v166, v126 offset:13328
	ds_write_b16 v166, v127 offset:13600
	ds_write_b16_d16_hi v166, v127 offset:13872
	ds_read_b128 v[126:129], v134 offset:45056
	ds_read_b128 v[154:157], v134 offset:45120
	ds_read_b128 v[158:161], v137 offset:256
	ds_read_b128 v[162:165], v137 offset:272
	ds_read_b128 v[166:169], v134 offset:47616
	ds_read_b128 v[170:173], v134 offset:47680
	ds_read_b128 v[174:177], v134 offset:50176
	ds_read_b128 v[178:181], v134 offset:50240
	ds_read_b128 v[182:185], v134 offset:52736
	ds_read_b128 v[220:223], v134 offset:52800
	ds_read_b128 v[224:227], v137 offset:384
	ds_read_b128 v[228:231], v137 offset:400
	s_waitcnt lgkmcnt(14)
	v_mul_f32_e32 v108, v108, v196
	v_mul_f32_e32 v109, v109, v197
	v_mul_f32_e32 v106, v106, v194
	v_mul_f32_e32 v107, v107, v195
	v_mul_f32_e32 v104, v104, v200
	v_mul_f32_e32 v105, v105, v201
	v_mul_f32_e32 v102, v102, v198
	v_mul_f32_e32 v103, v103, v199
	v_mul_f32_e32 v100, v100, v246
	v_mul_f32_e32 v101, v101, v247
	v_mul_f32_e32 v98, v98, v244
	v_mul_f32_e32 v99, v99, v245
	v_mul_f32_e32 v96, v96, v250
	v_mul_f32_e32 v97, v97, v251
	v_mul_f32_e32 v94, v94, v248
	v_mul_f32_e32 v95, v95, v249
	v_mfma_f32_16x16x32_bf16 v[106:109], v[186:189], v[46:49], v[106:109]
	v_mfma_f32_16x16x32_bf16 v[102:105], v[202:205], v[46:49], v[102:105]
	v_mfma_f32_16x16x32_bf16 v[98:101], v[210:213], v[46:49], v[98:101]
	v_mfma_f32_16x16x32_bf16 v[94:97], v[236:239], v[46:49], v[94:97]
	v_mfma_f32_16x16x32_bf16 v[106:109], v[190:193], v[30:33], v[106:109]
	v_mfma_f32_16x16x32_bf16 v[102:105], v[206:209], v[30:33], v[102:105]
	v_mfma_f32_16x16x32_bf16 v[98:101], v[216:219], v[30:33], v[98:101]
	v_mfma_f32_16x16x32_bf16 v[94:97], v[240:243], v[30:33], v[94:97]
	ds_read_b128 v[186:189], v134 offset:55296
	ds_read_b128 v[190:193], v134 offset:55360
	ds_read_b128 v[194:197], v137 offset:512
	ds_read_b128 v[198:201], v137 offset:528
	ds_read_b128 v[202:205], v134 offset:57856
	ds_read_b128 v[206:209], v134 offset:57920
	ds_read_b128 v[210:213], v134 offset:60416
	ds_read_b128 v[216:219], v134 offset:60480
	ds_read_b128 v[232:235], v134 offset:62976
	ds_read_b128 v[236:239], v134 offset:63040
	ds_read_b128 v[240:243], v137 offset:640
	ds_read_b128 v[244:247], v137 offset:656
	s_waitcnt lgkmcnt(14)
	v_mul_f32_e32 v92, v92, v160
	v_mul_f32_e32 v93, v93, v161
	v_mul_f32_e32 v90, v90, v158
	v_mul_f32_e32 v91, v91, v159
	v_mul_f32_e32 v88, v88, v164
	v_mul_f32_e32 v89, v89, v165
	v_mul_f32_e32 v86, v86, v162
	v_mul_f32_e32 v87, v87, v163
	s_waitcnt lgkmcnt(13)
	v_mul_f32_e32 v84, v84, v226
	v_mul_f32_e32 v85, v85, v227
	v_mul_f32_e32 v82, v82, v224
	v_mul_f32_e32 v83, v83, v225
	s_waitcnt lgkmcnt(12)
	v_mul_f32_e32 v80, v80, v230
	v_mul_f32_e32 v81, v81, v231
	v_mul_f32_e32 v78, v78, v228
	v_mul_f32_e32 v79, v79, v229
	v_mfma_f32_16x16x32_bf16 v[90:93], v[126:129], v[46:49], v[90:93]
	v_mfma_f32_16x16x32_bf16 v[86:89], v[166:169], v[46:49], v[86:89]
	v_mfma_f32_16x16x32_bf16 v[82:85], v[174:177], v[46:49], v[82:85]
	v_mfma_f32_16x16x32_bf16 v[78:81], v[182:185], v[46:49], v[78:81]
	v_mfma_f32_16x16x32_bf16 v[90:93], v[154:157], v[30:33], v[90:93]
	v_mfma_f32_16x16x32_bf16 v[86:89], v[170:173], v[30:33], v[86:89]
	v_mfma_f32_16x16x32_bf16 v[82:85], v[178:181], v[30:33], v[82:85]
	v_mfma_f32_16x16x32_bf16 v[78:81], v[220:223], v[30:33], v[78:81]
	ds_read_b128 v[126:129], v136 offset:30720
	ds_read_b128 v[154:157], v136 offset:30784
	ds_read_b128 v[158:161], v137 offset:768
	ds_read_b128 v[162:165], v137 offset:784
	ds_read_b128 v[166:169], v136 offset:33280
	ds_read_b128 v[170:173], v136 offset:33344
	ds_read_b128 v[174:177], v136 offset:35840
	ds_read_b128 v[178:181], v136 offset:35904
	ds_read_b128 v[182:185], v136 offset:38400
	ds_read_b128 v[220:223], v136 offset:38464
	ds_read_b128 v[224:227], v137 offset:896
	ds_read_b128 v[228:231], v137 offset:912
	s_waitcnt lgkmcnt(14)
	v_mul_f32_e32 v76, v76, v196
	v_mul_f32_e32 v77, v77, v197
	v_mul_f32_e32 v74, v74, v194
	v_mul_f32_e32 v75, v75, v195
	v_mul_f32_e32 v72, v72, v200
	v_mul_f32_e32 v73, v73, v201
	v_mul_f32_e32 v70, v70, v198
	v_mul_f32_e32 v71, v71, v199
	s_waitcnt lgkmcnt(13)
	v_mul_f32_e32 v68, v68, v242
	v_mul_f32_e32 v69, v69, v243
	v_mul_f32_e32 v66, v66, v240
	v_mul_f32_e32 v67, v67, v241
	s_waitcnt lgkmcnt(12)
	v_mul_f32_e32 v64, v64, v246
	v_mul_f32_e32 v65, v65, v247
	v_mul_f32_e32 v62, v62, v244
	v_mul_f32_e32 v63, v63, v245
	v_mfma_f32_16x16x32_bf16 v[74:77], v[186:189], v[46:49], v[74:77]
	v_mfma_f32_16x16x32_bf16 v[70:73], v[202:205], v[46:49], v[70:73]
	v_mfma_f32_16x16x32_bf16 v[66:69], v[210:213], v[46:49], v[66:69]
	v_mfma_f32_16x16x32_bf16 v[62:65], v[232:235], v[46:49], v[62:65]
	v_mfma_f32_16x16x32_bf16 v[74:77], v[190:193], v[30:33], v[74:77]
	v_mfma_f32_16x16x32_bf16 v[70:73], v[206:209], v[30:33], v[70:73]
	v_mfma_f32_16x16x32_bf16 v[66:69], v[216:219], v[30:33], v[66:69]
	v_mfma_f32_16x16x32_bf16 v[62:65], v[236:239], v[30:33], v[62:65]
	s_waitcnt lgkmcnt(9)
	v_mul_f32_e32 v60, v60, v160
	v_mul_f32_e32 v61, v61, v161
	v_mul_f32_e32 v58, v58, v158
	v_mul_f32_e32 v59, v59, v159
	s_waitcnt lgkmcnt(8)
	v_mul_f32_e32 v56, v56, v164
	v_mul_f32_e32 v57, v57, v165
	v_mul_f32_e32 v54, v54, v162
	v_mul_f32_e32 v55, v55, v163
	s_waitcnt lgkmcnt(1)
	v_mul_f32_e32 v52, v52, v226
	v_mul_f32_e32 v53, v53, v227
	v_mul_f32_e32 v50, v50, v224
	v_mul_f32_e32 v51, v51, v225
	s_waitcnt lgkmcnt(0)
	v_mul_f32_e32 v112, v112, v230
	v_mul_f32_e32 v113, v113, v231
	v_mul_f32_e32 v110, v110, v228
	v_mul_f32_e32 v111, v111, v229
	v_mfma_f32_16x16x32_bf16 v[58:61], v[126:129], v[46:49], v[58:61]
	s_add_i32 s15, s15, -1
	s_cmp_eq_u32 s15, 4
	s_mov_b32 s9, s22
	v_mfma_f32_16x16x32_bf16 v[54:57], v[166:169], v[46:49], v[54:57]
	v_mfma_f32_16x16x32_bf16 v[50:53], v[174:177], v[46:49], v[50:53]
	v_mfma_f32_16x16x32_bf16 v[46:49], v[182:185], v[46:49], v[110:113]
	v_mfma_f32_16x16x32_bf16 v[58:61], v[154:157], v[30:33], v[58:61]
	v_mfma_f32_16x16x32_bf16 v[54:57], v[170:173], v[30:33], v[54:57]
	v_mfma_f32_16x16x32_bf16 v[50:53], v[178:181], v[30:33], v[50:53]
	v_mfma_f32_16x16x32_bf16 v[110:113], v[220:223], v[30:33], v[46:49]
	s_waitcnt vmcnt(0)
	v_mov_b64_e32 v[30:31], v[118:119]
	v_mov_b64_e32 v[32:33], v[120:121]
	s_nop 0
	v_mov_b64_e32 v[46:47], v[114:115]
	v_mov_b64_e32 v[48:49], v[116:117]
	s_cbranch_scc1 .LBB0_619
